# v80 + retention chunk: barrier 2 removed (STL state writes deferred to after barrier 3, 2 barriers per chunk), tile writes still interleaved in the rope block
# baseline (speedup 1.0000x reference)
; #define LAS __attribute__((address_space(3)))
; #define LDS_BARRIER() do { asm volatile("s_waitcnt lgkmcnt(0)" ::: "memory"); __builtin_amdgcn_s_barrier(); asm volatile("" ::: "memory"); } while (0)
; template <int NET> __device__ __forceinline__ void ret_item(Ctx& F, int item) {
;     ...
;     for (int n = 0; n < 16; ++n) {
;         const int t0 = b * SEQ + n * 128;
;         RET_LOAD(n + 1 < 16 ? n + 1 : 15);
;         LDS_BARRIER();
;         f32x4 sacc[8];
; #pragma unroll
;         for (int mt = 0; mt < 8; ++mt) sacc[mt] = (f32x4){0.f, 0.f, 0.f, 0.f};
; #pragma unroll
;         for (int ks = 0; ks < 4; ++ks) { const bf16x8 bq = *(const LAS bf16x8*)(qL + (16 * w + fr) * LP + 32 * ks + 8 * fq);
; #pragma unroll
;             for (int mt = 0; mt < 8; ++mt) { const bf16x8 ak = *(const LAS bf16x8*)(kL + (16 * mt + fr) * LP + 32 * ks + 8 * fq); sacc[mt] = __builtin_amdgcn_mfma_f32_16x16x32_bf16(ak, bq, sacc[mt], 0, 0, 0); } }
.LBB0_314:
	s_add_i32 s74, s33, 0x80
	s_cmpk_eq_i32 s33, 0x780
	s_cselect_b32 s0, s33, s74
	v_add_u32_e32 v18, s0, v112
	v_mov_b64_e32 v[20:21], s[88:89]
	v_ashrrev_i32_e32 v19, 31, v18
	v_mad_i64_i32 v[20:21], s[0:1], v18, s91, v[20:21]
	v_lshlrev_b64 v[42:43], 8, v[18:19]
	v_lshl_add_u64 v[18:19], v[20:21], 0, v[106:107]
	global_load_dwordx4 v[26:29], v[18:19], off offset:16
	global_load_dwordx4 v[50:53], v[18:19], off
	global_load_dwordx4 v[30:33], v[18:19], off offset:144
	global_load_dwordx4 v[54:57], v[18:19], off offset:128
	global_load_dwordx4 v[34:37], v[18:19], off offset:2064
	global_load_dwordx4 v[58:61], v[18:19], off offset:2048
	global_load_dwordx4 v[38:41], v[18:19], off offset:2192
	global_load_dwordx4 v[62:65], v[18:19], off offset:2176
	v_lshl_add_u64 v[18:19], s[80:81], 1, v[20:21]
	v_lshl_add_u64 v[18:19], v[18:19], 0, v[106:107]
	v_lshl_add_u64 v[20:21], v[18:19], 0, s[78:79]
	v_add_co_u32_e64 v18, s[0:1], s92, v18
	v_lshl_add_u64 v[70:71], v[108:109], 0, v[42:43]
	s_nop 0
	v_addc_co_u32_e64 v19, s[0:1], 0, v19, s[0:1]
	global_load_dwordx4 v[22:25], v[18:19], off
	s_nop 0
	global_load_dwordx4 v[18:21], v[20:21], off offset:16
	s_nop 0
	global_load_dwordx4 v[42:45], v[70:71], off offset:48
	global_load_dwordx4 v[46:49], v[70:71], off offset:32
	global_load_dwordx4 v[66:69], v[70:71], off offset:16
	s_nop 0
	global_load_dwordx4 v[70:73], v[70:71], off
	s_waitcnt lgkmcnt(0)
	s_barrier
	ds_read_b128 v[74:77], v163
	ds_read_b128 v[78:81], v187 offset:34816
	ds_read_b128 v[82:85], v187 offset:39168
	ds_read_b128 v[86:89], v187 offset:43520
	ds_read_b128 v[90:93], v187 offset:47872
	ds_read_b128 v[94:97], v187 offset:52224
	ds_read_b128 v[98:101], v187 offset:56576
	ds_read_b128 v[102:105], v187 offset:60928
	ds_read_b128 v[232:235], v187 offset:65280
	s_waitcnt lgkmcnt(7)
	v_mfma_f32_16x16x32_bf16 v[78:81], v[78:81], v[74:77], 0
	v_add_u32_e32 v115, 0x1200, v166
	v_add_u32_e32 v130, 0x2400, v166
	v_add_u32_e32 v131, 0x3600, v166
	s_waitcnt lgkmcnt(6)
	v_mfma_f32_16x16x32_bf16 v[82:85], v[82:85], v[74:77], 0
	v_add_u32_e32 v132, 0x900, v166
	v_add_u32_e32 v133, 0x1b00, v166
	v_add_u32_e32 v248, 0x2d00, v166
	s_waitcnt lgkmcnt(5)
	v_mfma_f32_16x16x32_bf16 v[86:89], v[86:89], v[74:77], 0
	v_add_u32_e32 v249, 0x3f00, v166
	v_add_u32_e32 v124, s33, v111
	v_ashrrev_i32_e32 v125, 31, v124
	s_waitcnt lgkmcnt(4)
	v_mfma_f32_16x16x32_bf16 v[90:93], v[90:93], v[74:77], 0
	v_lshlrev_b64 v[124:125], 12, v[124:125]
	v_lshl_add_u64 v[124:125], v[120:121], 0, v[124:125]
	v_pk_mul_f32 v[10:11], v[122:123], v[10:11]
	s_waitcnt lgkmcnt(3)
	v_mfma_f32_16x16x32_bf16 v[94:97], v[94:97], v[74:77], 0
	v_mul_f32_e64 v14, v122, v14
	v_mul_f32_e64 v15, v123, v15
	v_pk_mul_f32 v[6:7], v[122:123], v[6:7]
	v_pk_mul_f32 v[2:3], v[122:123], v[2:3]
	s_waitcnt lgkmcnt(2)
	v_mfma_f32_16x16x32_bf16 v[98:101], v[98:101], v[74:77], 0
	s_cmpk_lg_i32 s74, 0x800
	s_mov_b32 s33, s74
	s_waitcnt lgkmcnt(1)
	v_mfma_f32_16x16x32_bf16 v[102:105], v[102:105], v[74:77], 0
	s_waitcnt lgkmcnt(0)
	v_mfma_f32_16x16x32_bf16 v[74:77], v[232:235], v[74:77], 0
	ds_read_b128 v[232:235], v163 offset:64
	ds_read_b128 v[236:239], v187 offset:34880
	s_waitcnt lgkmcnt(0)
	v_mfma_f32_16x16x32_bf16 v[78:81], v[236:239], v[232:235], v[78:81]
	ds_read_b128 v[236:239], v187 offset:39232
	s_waitcnt lgkmcnt(0)
	v_mfma_f32_16x16x32_bf16 v[82:85], v[236:239], v[232:235], v[82:85]
	ds_read_b128 v[236:239], v187 offset:43584
	s_waitcnt lgkmcnt(0)
	v_mfma_f32_16x16x32_bf16 v[86:89], v[236:239], v[232:235], v[86:89]
	ds_read_b128 v[236:239], v187 offset:47936
	s_waitcnt lgkmcnt(0)
	v_mfma_f32_16x16x32_bf16 v[90:93], v[236:239], v[232:235], v[90:93]
	ds_read_b128 v[236:239], v187 offset:52288
	s_waitcnt lgkmcnt(0)
	v_mfma_f32_16x16x32_bf16 v[94:97], v[236:239], v[232:235], v[94:97]
	ds_read_b128 v[236:239], v187 offset:56640
	s_waitcnt lgkmcnt(0)
	v_mfma_f32_16x16x32_bf16 v[98:101], v[236:239], v[232:235], v[98:101]
	ds_read_b128 v[236:239], v187 offset:60992
	s_waitcnt lgkmcnt(0)
	v_mfma_f32_16x16x32_bf16 v[102:105], v[236:239], v[232:235], v[102:105]
	ds_read_b128 v[236:239], v187 offset:65344
	s_waitcnt lgkmcnt(0)
	v_mfma_f32_16x16x32_bf16 v[74:77], v[236:239], v[232:235], v[74:77]
	ds_read_b128 v[232:235], v163 offset:128
	ds_read_b128 v[236:239], v187 offset:34944
	s_waitcnt lgkmcnt(0)
	v_mfma_f32_16x16x32_bf16 v[78:81], v[236:239], v[232:235], v[78:81]
	ds_read_b128 v[236:239], v187 offset:39296
	s_waitcnt lgkmcnt(0)
	v_mfma_f32_16x16x32_bf16 v[82:85], v[236:239], v[232:235], v[82:85]
	ds_read_b128 v[236:239], v187 offset:43648
	s_waitcnt lgkmcnt(0)
	v_mfma_f32_16x16x32_bf16 v[86:89], v[236:239], v[232:235], v[86:89]
	ds_read_b128 v[236:239], v187 offset:48000
	s_waitcnt lgkmcnt(0)
	v_mfma_f32_16x16x32_bf16 v[90:93], v[236:239], v[232:235], v[90:93]
	ds_read_b128 v[236:239], v187 offset:52352
	s_waitcnt lgkmcnt(0)
	v_mfma_f32_16x16x32_bf16 v[94:97], v[236:239], v[232:235], v[94:97]
	ds_read_b128 v[236:239], v187 offset:56704
	s_waitcnt lgkmcnt(0)
	v_mfma_f32_16x16x32_bf16 v[98:101], v[236:239], v[232:235], v[98:101]
	ds_read_b128 v[236:239], v187 offset:61056
	s_waitcnt lgkmcnt(0)
	v_mfma_f32_16x16x32_bf16 v[102:105], v[236:239], v[232:235], v[102:105]
	ds_read_b128 v[236:239], v187 offset:65408
	s_waitcnt lgkmcnt(0)
	v_mfma_f32_16x16x32_bf16 v[74:77], v[236:239], v[232:235], v[74:77]
	ds_read_b128 v[232:235], v163 offset:192
	ds_read_b128 v[236:239], v187 offset:35008
	s_waitcnt lgkmcnt(0)
	v_mfma_f32_16x16x32_bf16 v[78:81], v[236:239], v[232:235], v[78:81]
	ds_read_b128 v[236:239], v187 offset:39360
	s_waitcnt lgkmcnt(0)
; #define LAS __attribute__((address_space(3)))
; __device__ __forceinline__ unsigned pk2(float lo, float hi) { unsigned r; asm volatile("v_cvt_pk_bf16_f32 %0, %1, %2" : "=v"(r) : "v"(lo), "v"(hi)); return r; }
; template <int NET> __device__ __forceinline__ void ret_item(Ctx& F, int item) {
;     ...
;         for (int ks = 0; ks < 4; ++ks) { const bf16x8 bq = *(const LAS bf16x8*)(qL + (16 * w + fr) * LP + 32 * ks + 8 * fq);
; #pragma unroll
;             for (int mt = 0; mt < 8; ++mt) { const bf16x8 ak = *(const LAS bf16x8*)(kL + (16 * mt + fr) * LP + 32 * ks + 8 * fq); sacc[mt] = __builtin_amdgcn_mfma_f32_16x16x32_bf16(ak, bq, sacc[mt], 0, 0, 0); } }
;         const int c = 16 * w + fr;
;         bf16x8 pb[4];
; #pragma unroll
;         for (int sk = 0; sk < 4; ++sk) { unsigned pw[4];
; #pragma unroll
;             for (int hlf = 0; hlf < 2; ++hlf) { const int mt = 2 * sk + hlf; float pv[4];
; #pragma unroll
;                 for (int rr = 0; rr < 4; ++rr) { const int m = 16 * mt + 4 * fq + rr; pv[rr] = (c >= m) ? sacc[mt][rr] * dcm[mt][rr] : 0.f; }
;                 pw[2 * hlf] = pk2(pv[0], pv[1]); pw[2 * hlf + 1] = pk2(pv[2], pv[3]); }
;             pb[sk] = __builtin_bit_cast(bf16x8, (u32x4){pw[0], pw[1], pw[2], pw[3]}); }
;         { bf16x8 bqf[4];
; #pragma unroll
;           for (int ks = 0; ks < 4; ++ks) bqf[ks] = *(const LAS bf16x8*)(qL + (16 * w + fr) * LP + 32 * ks + 8 * fq);
;           const float qd = __builtin_amdgcn_exp2f(lg2 * (float)(c + 1));
; #pragma unroll
;           for (int et = 0; et < NET; ++et) { f32x4 oi = (f32x4){0.f, 0.f, 0.f, 0.f}, oc = (f32x4){0.f, 0.f, 0.f, 0.f};
;             bf16x8 avq[4]; const unsigned a0 = vLb + (unsigned)((4 * fq) * (VP * 2) + 32 * et); tr_quad(avq, a0, a0 + 32 * (VP * 2), a0 + 64 * (VP * 2), a0 + 96 * (VP * 2), 16 * (VP * 2));
; #pragma unroll
;             for (int ks = 0; ks < 4; ++ks) { const bf16x8 as = *(const LAS bf16x8*)(STL + (16 * et + fr) * LP + 32 * ks + 8 * fq);
;                 oi = __builtin_amdgcn_mfma_f32_16x16x32_bf16(avq[ks], pb[ks], oi, 0, 0, 0); oc = __builtin_amdgcn_mfma_f32_16x16x32_bf16(as, bqf[ks], oc, 0, 0, 0); }
;             *(f32x4*)(reto + (size_t)(t0 + c) * RW + h * 128 + eb * EW + 16 * et + 4 * fq) = oi + oc * qd; } }
	v_mfma_f32_16x16x32_bf16 v[82:85], v[236:239], v[232:235], v[82:85]
	ds_read_b128 v[236:239], v187 offset:43712
	s_waitcnt lgkmcnt(0)
	v_mfma_f32_16x16x32_bf16 v[86:89], v[236:239], v[232:235], v[86:89]
	ds_read_b128 v[236:239], v187 offset:48064
	s_waitcnt lgkmcnt(0)
	v_mfma_f32_16x16x32_bf16 v[90:93], v[236:239], v[232:235], v[90:93]
	ds_read_b128 v[236:239], v187 offset:52416
	s_waitcnt lgkmcnt(0)
	v_mfma_f32_16x16x32_bf16 v[94:97], v[236:239], v[232:235], v[94:97]
	ds_read_b128 v[236:239], v187 offset:56768
	s_waitcnt lgkmcnt(0)
	v_mfma_f32_16x16x32_bf16 v[98:101], v[236:239], v[232:235], v[98:101]
	ds_read_b128 v[236:239], v187 offset:61120
	s_waitcnt lgkmcnt(0)
	v_mfma_f32_16x16x32_bf16 v[102:105], v[236:239], v[232:235], v[102:105]
	ds_read_b128 v[236:239], v187 offset:65472
	s_waitcnt lgkmcnt(0)
	v_mfma_f32_16x16x32_bf16 v[232:235], v[236:239], v[232:235], v[74:77]
	s_nop 2
	v_mul_f32_e32 v74, v196, v78
	v_mul_f32_e32 v75, v197, v79
	v_mul_f32_e32 v76, v198, v80
	v_mul_f32_e32 v77, v199, v81
	v_cndmask_b32_e64 v74, v74, 0, vcc
	v_cndmask_b32_e64 v75, 0, v75, s[66:67]
	v_cndmask_b32_e64 v76, v76, 0, s[4:5]
	v_cndmask_b32_e64 v77, v77, 0, s[6:7]
	v_cvt_pk_bf16_f32 v74, v74, v75
	v_cvt_pk_bf16_f32 v75, v76, v77
	v_mul_f32_e32 v76, v200, v82
	v_mul_f32_e32 v77, v201, v83
	v_mul_f32_e32 v78, v202, v84
	v_mul_f32_e32 v79, v203, v85
	v_cndmask_b32_e64 v76, v76, 0, s[8:9]
	v_cndmask_b32_e64 v77, v77, 0, s[10:11]
	v_cndmask_b32_e64 v78, v78, 0, s[12:13]
	v_cndmask_b32_e64 v79, v79, 0, s[14:15]
	v_cvt_pk_bf16_f32 v76, v76, v77
	v_cvt_pk_bf16_f32 v77, v78, v79
	v_mul_f32_e32 v78, v204, v86
	v_mul_f32_e32 v79, v205, v87
	v_mul_f32_e32 v80, v206, v88
	v_mul_f32_e32 v81, v207, v89
	v_cndmask_b32_e64 v78, v78, 0, s[16:17]
	v_cndmask_b32_e64 v79, v79, 0, s[18:19]
	v_cndmask_b32_e64 v80, v80, 0, s[20:21]
	v_cndmask_b32_e64 v81, v81, 0, s[22:23]
	v_cvt_pk_bf16_f32 v78, v78, v79
	v_cvt_pk_bf16_f32 v79, v80, v81
	v_mul_f32_e32 v80, v208, v90
	v_mul_f32_e32 v81, v209, v91
	v_mul_f32_e32 v82, v210, v92
	v_mul_f32_e32 v83, v211, v93
	v_cndmask_b32_e64 v80, v80, 0, s[24:25]
	v_cndmask_b32_e64 v81, v81, 0, s[26:27]
	v_cndmask_b32_e64 v82, v82, 0, s[28:29]
	v_cndmask_b32_e64 v83, v83, 0, s[30:31]
	v_cvt_pk_bf16_f32 v80, v80, v81
	v_cvt_pk_bf16_f32 v81, v82, v83
	v_mul_f32_e32 v82, v212, v94
	v_mul_f32_e32 v83, v213, v95
	v_mul_f32_e32 v84, v214, v96
	v_mul_f32_e32 v85, v215, v97
	v_cndmask_b32_e64 v82, v82, 0, s[34:35]
	v_cndmask_b32_e64 v83, v83, 0, s[36:37]
	v_cndmask_b32_e64 v84, v84, 0, s[38:39]
	v_cndmask_b32_e64 v85, v85, 0, s[40:41]
	v_cvt_pk_bf16_f32 v82, v82, v83
	v_cvt_pk_bf16_f32 v83, v84, v85
	v_mul_f32_e32 v84, v216, v98
	v_mul_f32_e32 v85, v217, v99
	v_mul_f32_e32 v86, v218, v100
	v_mul_f32_e32 v87, v219, v101
	v_cndmask_b32_e64 v84, v84, 0, s[42:43]
	v_cndmask_b32_e64 v85, v85, 0, s[44:45]
	v_cndmask_b32_e64 v86, v86, 0, s[46:47]
	v_cndmask_b32_e64 v87, v87, 0, s[48:49]
	v_cvt_pk_bf16_f32 v84, v84, v85
	v_cvt_pk_bf16_f32 v85, v86, v87
	v_mul_f32_e32 v86, v220, v102
	v_mul_f32_e32 v87, v221, v103
	v_mul_f32_e32 v88, v222, v104
	v_mul_f32_e32 v89, v223, v105
	v_cndmask_b32_e64 v86, v86, 0, s[50:51]
	v_cndmask_b32_e64 v87, v87, 0, s[52:53]
	v_cndmask_b32_e64 v88, v88, 0, s[54:55]
	v_cndmask_b32_e64 v89, v89, 0, s[56:57]
	v_cvt_pk_bf16_f32 v86, v86, v87
	v_cvt_pk_bf16_f32 v87, v88, v89
	v_mul_f32_e32 v88, v224, v232
	v_mul_f32_e32 v89, v225, v233
	v_mul_f32_e32 v90, v226, v234
	v_cndmask_b32_e64 v88, v88, 0, s[58:59]
	v_cndmask_b32_e64 v89, v89, 0, s[60:61]
	v_cndmask_b32_e64 v90, v90, 0, s[62:63]
	v_mul_f32_e32 v91, v113, v235
	v_cndmask_b32_e64 v91, v91, 0, s[64:65]
	v_cvt_pk_bf16_f32 v88, v88, v89
	v_cvt_pk_bf16_f32 v89, v90, v91
	v_add_u32_e32 v90, v162, v164
	ds_read_b128 v[102:105], v90
	ds_read_b128 v[98:101], v90 offset:64
	ds_read_b128 v[94:97], v90 offset:128
	ds_read_b128 v[90:93], v90 offset:192
	ds_read_b64_tr_b16 v[244:245], v166
	ds_read_b64_tr_b16 v[246:247], v132
	ds_read_b64_tr_b16 v[240:241], v115
	ds_read_b64_tr_b16 v[242:243], v133
	ds_read_b64_tr_b16 v[236:237], v130
	ds_read_b64_tr_b16 v[238:239], v248
	ds_read_b64_tr_b16 v[232:233], v131
	ds_read_b64_tr_b16 v[234:235], v249
	s_waitcnt lgkmcnt(0)
	ds_read_b128 v[248:251], v188
	ds_read_b128 v[130:133], v188 offset:64
	v_mfma_f32_16x16x32_bf16 v[244:247], v[244:247], v[74:77], 0
	v_add_u32_e32 v115, 32, v166
	v_mfma_f32_16x16x32_bf16 v[240:243], v[240:243], v[78:81], v[244:247]
	s_waitcnt lgkmcnt(1)
	v_mfma_f32_16x16x32_bf16 v[248:251], v[248:251], v[102:105], 0
	s_nop 3
	ds_read_b128 v[244:247], v188 offset:128
	v_mfma_f32_16x16x32_bf16 v[236:239], v[236:239], v[82:85], v[240:243]
	s_nop 2
	ds_read_b128 v[240:243], v188 offset:192
	s_waitcnt lgkmcnt(2)
	v_mfma_f32_16x16x32_bf16 v[130:133], v[130:133], v[98:101], v[248:251]
	s_waitcnt lgkmcnt(1)
	v_mfma_f32_16x16x32_bf16 v[130:133], v[244:247], v[94:97], v[130:133]
	v_add_u32_e32 v244, 0x1220, v166
	v_add_u32_e32 v245, 0x2420, v166
	v_add_u32_e32 v246, 0x3620, v166
	v_mfma_f32_16x16x32_bf16 v[232:235], v[232:235], v[86:89], v[236:239]
	v_add_u32_e32 v247, 0x920, v166
	v_add_u32_e32 v248, 0x1b20, v166
	v_add_u32_e32 v249, 0x2d20, v166
	s_waitcnt lgkmcnt(0)
	v_mfma_f32_16x16x32_bf16 v[130:133], v[240:243], v[90:93], v[130:133]
	v_add_u32_e32 v250, 0x3f20, v166
	s_nop 6
	v_pk_fma_f32 v[132:133], v[118:119], v[132:133], v[234:235]
	v_pk_fma_f32 v[130:131], v[116:117], v[130:131], v[232:233]
	global_store_dwordx4 v[124:125], v[130:133], off
	s_nop 1
	ds_read_b64_tr_b16 v[240:241], v115
	ds_read_b64_tr_b16 v[242:243], v247
	ds_read_b64_tr_b16 v[236:237], v244
	ds_read_b64_tr_b16 v[238:239], v248
	ds_read_b64_tr_b16 v[232:233], v245
	ds_read_b64_tr_b16 v[234:235], v249
	ds_read_b64_tr_b16 v[130:131], v246
	ds_read_b64_tr_b16 v[132:133], v250
	s_waitcnt lgkmcnt(0)
; #define LAS __attribute__((address_space(3)))
; #define LDS_BARRIER() do { asm volatile("s_waitcnt lgkmcnt(0)" ::: "memory"); __builtin_amdgcn_s_barrier(); asm volatile("" ::: "memory"); } while (0)
; template <int NET> __device__ __forceinline__ void ret_item(Ctx& F, int item) {
;     ...
;           for (int et = 0; et < NET; ++et) { f32x4 oi = (f32x4){0.f, 0.f, 0.f, 0.f}, oc = (f32x4){0.f, 0.f, 0.f, 0.f};
;             bf16x8 avq[4]; const unsigned a0 = vLb + (unsigned)((4 * fq) * (VP * 2) + 32 * et); tr_quad(avq, a0, a0 + 32 * (VP * 2), a0 + 64 * (VP * 2), a0 + 96 * (VP * 2), 16 * (VP * 2));
; #pragma unroll
;             for (int ks = 0; ks < 4; ++ks) { const bf16x8 as = *(const LAS bf16x8*)(STL + (16 * et + fr) * LP + 32 * ks + 8 * fq);
;                 oi = __builtin_amdgcn_mfma_f32_16x16x32_bf16(avq[ks], pb[ks], oi, 0, 0, 0); oc = __builtin_amdgcn_mfma_f32_16x16x32_bf16(as, bqf[ks], oc, 0, 0, 0); }
;             *(f32x4*)(reto + (size_t)(t0 + c) * RW + h * 128 + eb * EW + 16 * et + 4 * fq) = oi + oc * qd; } }
;         LDS_BARRIER();
; #pragma unroll
;         for (int et = 0; et < NET; ++et) st[et] = st[et] * dec;
;         { bf16x8 bkq[4];
;           { const unsigned k0 = kLb + (unsigned)((8 * fq) * (LP * 2)); tr_quad(bkq, k0, k0 + 32 * (LP * 2), k0 + 64 * (LP * 2), k0 + 96 * (LP * 2), 4 * (LP * 2)); }
; #pragma unroll
;           for (int et = 0; et < NET; ++et) { bf16x8 vq[4]; const unsigned v0 = vdLb + (unsigned)((8 * fq) * (VP * 2) + 32 * et); tr_quad(vq, v0, v0 + 32 * (VP * 2), v0 + 64 * (VP * 2), v0 + 96 * (VP * 2), 4 * (VP * 2));
	ds_read_b128 v[244:247], v188 offset:4352
	ds_read_b128 v[248:251], v188 offset:4416
	v_mfma_f32_16x16x32_bf16 v[240:243], v[240:243], v[74:77], 0
	v_add_u32_e32 v115, 64, v166
	s_waitcnt lgkmcnt(1)
	v_mfma_f32_16x16x32_bf16 v[244:247], v[244:247], v[102:105], 0
	v_mfma_f32_16x16x32_bf16 v[236:239], v[236:239], v[78:81], v[240:243]
	s_waitcnt lgkmcnt(0)
	v_mfma_f32_16x16x32_bf16 v[240:243], v[248:251], v[98:101], v[244:247]
	v_add_u32_e32 v248, 0x1b40, v166
	v_add_u32_e32 v249, 0x2d40, v166
	v_add_u32_e32 v250, 0x3f40, v166
	s_nop 1
	ds_read_b128 v[244:247], v188 offset:4480
	v_mfma_f32_16x16x32_bf16 v[232:235], v[232:235], v[82:85], v[236:239]
	s_waitcnt lgkmcnt(0)
	v_mfma_f32_16x16x32_bf16 v[236:239], v[244:247], v[94:97], v[240:243]
	s_nop 2
	ds_read_b128 v[240:243], v188 offset:4544
	v_add_u32_e32 v244, 0x1240, v166
	v_add_u32_e32 v245, 0x2440, v166
	v_mfma_f32_16x16x32_bf16 v[130:133], v[130:133], v[86:89], v[232:235]
	v_add_u32_e32 v246, 0x3640, v166
	v_add_u32_e32 v247, 0x940, v166
	s_waitcnt lgkmcnt(0)
	v_mfma_f32_16x16x32_bf16 v[232:235], v[240:243], v[90:93], v[236:239]
	s_nop 7
	v_pk_fma_f32 v[132:133], v[118:119], v[234:235], v[132:133]
	v_pk_fma_f32 v[130:131], v[116:117], v[232:233], v[130:131]
	global_store_dwordx4 v[124:125], v[130:133], off offset:64
	s_nop 1
	ds_read_b64_tr_b16 v[240:241], v115
	ds_read_b64_tr_b16 v[242:243], v247
	ds_read_b64_tr_b16 v[236:237], v244
	ds_read_b64_tr_b16 v[238:239], v248
	ds_read_b64_tr_b16 v[232:233], v245
	ds_read_b64_tr_b16 v[234:235], v249
	ds_read_b64_tr_b16 v[130:131], v246
	ds_read_b64_tr_b16 v[132:133], v250
	s_waitcnt lgkmcnt(0)
	ds_read_b128 v[244:247], v188 offset:8704
	ds_read_b128 v[248:251], v188 offset:8768
	v_mfma_f32_16x16x32_bf16 v[240:243], v[240:243], v[74:77], 0
	v_add_u32_e32 v115, 0x60, v166
	s_waitcnt lgkmcnt(1)
	v_mfma_f32_16x16x32_bf16 v[244:247], v[244:247], v[102:105], 0
	v_mfma_f32_16x16x32_bf16 v[236:239], v[236:239], v[78:81], v[240:243]
	s_waitcnt lgkmcnt(0)
	v_mfma_f32_16x16x32_bf16 v[240:243], v[248:251], v[98:101], v[244:247]
	v_add_u32_e32 v248, 0x1b60, v166
	v_add_u32_e32 v249, 0x2d60, v166
	v_add_u32_e32 v250, 0x3f60, v166
	s_nop 1
	ds_read_b128 v[244:247], v188 offset:8832
	v_mfma_f32_16x16x32_bf16 v[232:235], v[232:235], v[82:85], v[236:239]
	s_waitcnt lgkmcnt(0)
	v_mfma_f32_16x16x32_bf16 v[236:239], v[244:247], v[94:97], v[240:243]
	s_nop 2
	ds_read_b128 v[240:243], v188 offset:8896
	v_add_u32_e32 v244, 0x1260, v166
	v_add_u32_e32 v245, 0x2460, v166
	v_mfma_f32_16x16x32_bf16 v[130:133], v[130:133], v[86:89], v[232:235]
	v_add_u32_e32 v246, 0x3660, v166
	v_add_u32_e32 v247, 0x960, v166
	s_waitcnt lgkmcnt(0)
	v_mfma_f32_16x16x32_bf16 v[232:235], v[240:243], v[90:93], v[236:239]
	s_nop 7
	v_pk_fma_f32 v[132:133], v[118:119], v[234:235], v[132:133]
	v_pk_fma_f32 v[130:131], v[116:117], v[232:233], v[130:131]
	global_store_dwordx4 v[124:125], v[130:133], off offset:128
	s_nop 1
	ds_read_b64_tr_b16 v[240:241], v115
	ds_read_b64_tr_b16 v[242:243], v247
	ds_read_b64_tr_b16 v[236:237], v244
	ds_read_b64_tr_b16 v[238:239], v248
	ds_read_b64_tr_b16 v[232:233], v245
	ds_read_b64_tr_b16 v[234:235], v249
	ds_read_b64_tr_b16 v[130:131], v246
	ds_read_b64_tr_b16 v[132:133], v250
	s_waitcnt lgkmcnt(0)
	ds_read_b128 v[244:247], v188 offset:13056
	v_mfma_f32_16x16x32_bf16 v[74:77], v[240:243], v[74:77], 0
	ds_read_b128 v[240:243], v188 offset:13120
	v_mov_b32_e32 v115, v114
	v_pk_mul_f32 v[12:13], v[114:115], v[12:13]
	s_waitcnt lgkmcnt(1)
	v_mfma_f32_16x16x32_bf16 v[102:105], v[244:247], v[102:105], 0
	v_mul_f32_e64 v16, v114, v16
	v_mul_f32_e64 v17, v115, v17
	v_pk_mul_f32 v[8:9], v[114:115], v[8:9]
	v_pk_mul_f32 v[4:5], v[114:115], v[4:5]
	v_mfma_f32_16x16x32_bf16 v[74:77], v[236:239], v[78:81], v[74:77]
	v_add_u32_e32 v115, 0x1200, v168
	s_waitcnt lgkmcnt(0)
	v_mfma_f32_16x16x32_bf16 v[78:81], v[240:243], v[98:101], v[102:105]
	ds_read_b128 v[98:101], v188 offset:13184
	v_mfma_f32_16x16x32_bf16 v[74:77], v[232:235], v[82:85], v[74:77]
	ds_read_b128 v[82:85], v188 offset:13248
	v_add_u32_e32 v232, 0x3860, v168
	s_waitcnt lgkmcnt(1)
	v_mfma_f32_16x16x32_bf16 v[78:81], v[98:101], v[94:97], v[78:81]
	v_add_u32_e32 v94, 0x2640, v167
	v_add_u32_e32 v95, 0x4840, v167
	v_add_u32_e32 v96, 0x6a40, v167
	v_mfma_f32_16x16x32_bf16 v[74:77], v[130:133], v[86:89], v[74:77]
	v_add_u32_e32 v130, 0x240, v168
	v_add_u32_e32 v131, 0x1440, v168
	v_add_u32_e32 v132, 0x2640, v168
	s_waitcnt lgkmcnt(0)
	v_mfma_f32_16x16x32_bf16 v[78:81], v[82:85], v[90:93], v[78:81]
	v_add_u32_e32 v90, 0x2200, v167
	v_add_u32_e32 v91, 0x4400, v167
	v_add_u32_e32 v92, 0x6600, v167
	v_add_u32_e32 v93, 0x440, v167
	v_add_u32_e32 v133, 0x3840, v168
	s_nop 2
	v_pk_fma_f32 v[76:77], v[118:119], v[80:81], v[76:77]
	v_pk_fma_f32 v[74:75], v[116:117], v[78:79], v[74:75]
	global_store_dwordx4 v[124:125], v[74:77], off offset:192
	v_add_u32_e32 v124, 0x2400, v168
	ds_read_b64_tr_b16 v[86:87], v167
	ds_read_b64_tr_b16 v[88:89], v93
	ds_read_b64_tr_b16 v[82:83], v90
	ds_read_b64_tr_b16 v[84:85], v94
	ds_read_b64_tr_b16 v[78:79], v91
	ds_read_b64_tr_b16 v[80:81], v95
	ds_read_b64_tr_b16 v[74:75], v92
	ds_read_b64_tr_b16 v[76:77], v96
	s_waitcnt lgkmcnt(0)
	v_add_u32_e32 v125, 0x3600, v168
	ds_read_b64_tr_b16 v[102:103], v168
	ds_read_b64_tr_b16 v[104:105], v130
	ds_read_b64_tr_b16 v[98:99], v115
	ds_read_b64_tr_b16 v[100:101], v131
	ds_read_b64_tr_b16 v[94:95], v124
	ds_read_b64_tr_b16 v[96:97], v132
	ds_read_b64_tr_b16 v[90:91], v125
	ds_read_b64_tr_b16 v[92:93], v133
	s_waitcnt lgkmcnt(0)
; #define LAS __attribute__((address_space(3)))
; template <int NET> __device__ __forceinline__ void ret_item(Ctx& F, int item) {
;     ...
;             for (int hh = 0; hh < 2; ++hh) { unsigned oq1[4], oq2[4], ok1[4], ok2[4];
; #pragma unroll
;                 for (int c = 0; c < 4; ++c) { float a[2], bq[2], ka[2], kb[2];
; #pragma unroll
;                     for (int z = 0; z < 2; ++z) { const int jj = hh * 8 + c * 2 + z; const unsigned cw_ = cs4[jj >> 2][jj & 3]; const f32x2 sc = (f32x2){bflo(cw_), bfhi(cw_)};
;                         const float x1 = z ? bfhi(q1[hh][c]) : bflo(q1[hh][c]), x2 = z ? bfhi(q2[hh][c]) : bflo(q2[hh][c]);
;                         const float y1 = z ? bfhi(k1[hh][c]) : bflo(k1[hh][c]), y2 = z ? bfhi(k2[hh][c]) : bflo(k2[hh][c]);
;                         a[z] = (x1 * sc.x - x2 * sc.y) * 0.08838834764831845f; bq[z] = (x2 * sc.x + x1 * sc.y) * 0.08838834764831845f;
;                         ka[z] = y1 * sc.x - y2 * sc.y; kb[z] = y2 * sc.x + y1 * sc.y;
;                     }
;                     oq1[c] = pk2(a[0], a[1]); oq2[c] = pk2(bq[0], bq[1]); ok1[c] = pk2(ka[0], ka[1]); ok2[c] = pk2(kb[0], kb[1]); }
;                 *(LAS u32x4*)(qL + r * LP + j0 + hh * 8) = (u32x4){oq1[0], oq1[1], oq1[2], oq1[3]}; *(LAS u32x4*)(qL + r * LP + 64 + j0 + hh * 8) = (u32x4){oq2[0], oq2[1], oq2[2], oq2[3]};
;                 *(LAS u32x4*)(kL + r * LP + j0 + hh * 8) = (u32x4){ok1[0], ok1[1], ok1[2], ok1[3]}; *(LAS u32x4*)(kL + r * LP + 64 + j0 + hh * 8) = (u32x4){ok2[0], ok2[1], ok2[2], ok2[3]}; }
; #pragma unroll
;             for (int vi = 0; vi < NET / 2; ++vi) { unsigned vd[4];
; #pragma unroll
;                 for (int c = 0; c < 4; ++c) vd[c] = pk2(bflo(vv[vi][c]) * kdec, bfhi(vv[vi][c]) * kdec);
;     ...
;           for (int et = 0; et < NET; ++et) { bf16x8 vq[4]; const unsigned v0 = vdLb + (unsigned)((8 * fq) * (VP * 2) + 32 * et); tr_quad(vq, v0, v0 + 32 * (VP * 2), v0 + 64 * (VP * 2), v0 + 96 * (VP * 2), 4 * (VP * 2));
; #pragma unroll
;             for (int ks = 0; ks < 4; ++ks) st[et] = __builtin_amdgcn_mfma_f32_16x16x32_bf16(vq[ks], bkq[ks], st[et], 0, 0, 0); } }
; #pragma unroll
;         for (int et = 0; et < NET; ++et)
; #pragma unroll
;             for (int rr = 0; rr < 4; ++rr) STL[(16 * et + 4 * fq + rr) * LP + 16 * w + fr] = f2bf(st[et][rr]);
;         LDS_BARRIER();
;         ret_stage();
	v_add_u32_e32 v115, 32, v168
	v_mfma_f32_16x16x32_bf16 v[10:13], v[102:105], v[86:89], v[10:13]
	v_add_u32_e32 v124, 0x1220, v168
	v_add_u32_e32 v125, 0x2420, v168
	v_add_u32_e32 v130, 0x3620, v168
	v_mfma_f32_16x16x32_bf16 v[10:13], v[98:101], v[82:85], v[10:13]
	v_add_u32_e32 v131, 0x260, v168
	v_add_u32_e32 v132, 0x1460, v168
	v_add_u32_e32 v133, 0x2660, v168
	v_mfma_f32_16x16x32_bf16 v[10:13], v[94:97], v[78:81], v[10:13]
	v_mfma_f32_16x16x32_bf16 v[10:13], v[90:93], v[74:77], v[10:13]
	ds_read_b64_tr_b16 v[102:103], v115
	ds_read_b64_tr_b16 v[104:105], v131
	ds_read_b64_tr_b16 v[98:99], v124
	ds_read_b64_tr_b16 v[100:101], v132
	ds_read_b64_tr_b16 v[94:95], v125
	ds_read_b64_tr_b16 v[96:97], v133
	ds_read_b64_tr_b16 v[90:91], v130
	ds_read_b64_tr_b16 v[92:93], v232
	s_waitcnt lgkmcnt(0)
	v_add_u32_e32 v115, 64, v168
	v_mfma_f32_16x16x32_bf16 v[14:17], v[102:105], v[86:89], v[14:17]
	v_mfma_f32_16x16x32_bf16 v[14:17], v[98:101], v[82:85], v[14:17]
	v_mfma_f32_16x16x32_bf16 v[14:17], v[94:97], v[78:81], v[14:17]
	v_mfma_f32_16x16x32_bf16 v[14:17], v[90:93], v[74:77], v[14:17]
	ds_read_b64_tr_b16 v[102:103], v115
	ds_read_b64_tr_b16 v[104:105], v172
	ds_read_b64_tr_b16 v[98:99], v169
	ds_read_b64_tr_b16 v[100:101], v173
	ds_read_b64_tr_b16 v[94:95], v170
	ds_read_b64_tr_b16 v[96:97], v174
	ds_read_b64_tr_b16 v[90:91], v171
	ds_read_b64_tr_b16 v[92:93], v175
	s_waitcnt lgkmcnt(0)
	s_nop 0
	v_mfma_f32_16x16x32_bf16 v[6:9], v[102:105], v[86:89], v[6:9]
	v_mfma_f32_16x16x32_bf16 v[6:9], v[98:101], v[82:85], v[6:9]
	v_mfma_f32_16x16x32_bf16 v[6:9], v[94:97], v[78:81], v[6:9]
	v_mfma_f32_16x16x32_bf16 v[6:9], v[90:93], v[74:77], v[6:9]
	ds_read_b64_tr_b16 v[102:103], v176
	ds_read_b64_tr_b16 v[104:105], v180
	ds_read_b64_tr_b16 v[98:99], v177
	ds_read_b64_tr_b16 v[100:101], v181
	ds_read_b64_tr_b16 v[94:95], v178
	ds_read_b64_tr_b16 v[96:97], v182
	ds_read_b64_tr_b16 v[90:91], v179
	ds_read_b64_tr_b16 v[92:93], v183
	s_waitcnt lgkmcnt(0)
	s_nop 0
	v_mfma_f32_16x16x32_bf16 v[2:5], v[102:105], v[86:89], v[2:5]
	v_mfma_f32_16x16x32_bf16 v[2:5], v[98:101], v[82:85], v[2:5]
	v_mfma_f32_16x16x32_bf16 v[2:5], v[94:97], v[78:81], v[2:5]
	v_mfma_f32_16x16x32_bf16 v[2:5], v[90:93], v[74:77], v[2:5]
	s_waitcnt vmcnt(14)
	v_lshlrev_b32_e32 v79, 16, v54
	v_lshlrev_b32_e32 v78, 16, v50
	s_waitcnt vmcnt(4)
	v_and_b32_e32 v74, 0xffff0000, v70
	v_lshlrev_b32_e32 v75, 16, v70
	v_pk_mul_f32 v[80:81], v[74:75], v[78:79] op_sel:[1,0] op_sel_hi:[0,1]
	v_sub_f32_e32 v70, v80, v81
	v_pk_mul_f32 v[78:79], v[78:79], v[74:75]
	v_lshlrev_b32_e32 v77, 16, v62
	v_lshlrev_b32_e32 v76, 16, v58
	v_mul_f32_e32 v80, 0x3db504f3, v70
	v_add_f32_e32 v70, v78, v79
	v_mul_f32_e32 v81, 0x3db504f3, v70
	v_pk_mul_f32 v[78:79], v[74:75], v[76:77] op_sel:[1,0] op_sel_hi:[0,1]
	v_pk_mul_f32 v[74:75], v[76:77], v[74:75]
	v_and_b32_e32 v70, 0xffff0000, v71
	v_lshlrev_b32_e32 v71, 16, v71
	v_and_b32_e32 v77, 0xffff0000, v54
	v_and_b32_e32 v76, 0xffff0000, v50
	v_sub_f32_e32 v82, v78, v79
	v_add_f32_e32 v83, v74, v75
	v_and_b32_e32 v75, 0xffff0000, v62
	v_and_b32_e32 v74, 0xffff0000, v58
	v_pk_mul_f32 v[78:79], v[70:71], v[76:77] op_sel:[1,0] op_sel_hi:[0,1]
	v_pk_mul_f32 v[76:77], v[76:77], v[70:71]
	v_sub_f32_e32 v50, v78, v79
	v_add_f32_e32 v54, v76, v77
	v_pk_mul_f32 v[76:77], v[70:71], v[74:75] op_sel:[1,0] op_sel_hi:[0,1]
	v_pk_mul_f32 v[70:71], v[74:75], v[70:71]
	v_mul_f32_e32 v50, 0x3db504f3, v50
	v_mul_f32_e32 v54, 0x3db504f3, v54
	v_sub_f32_e32 v76, v76, v77
	v_add_f32_e32 v70, v70, v71
	s_waitcnt lgkmcnt(0)
	s_barrier
	v_cvt_pk_bf16_f32 v74, v10, s0
	ds_write_b16 v189, v74
	v_cvt_pk_bf16_f32 v74, v11, s0
	ds_write_b16 v190, v74
	v_cvt_pk_bf16_f32 v74, v12, s0
	ds_write_b16 v190, v74 offset:272
	v_cvt_pk_bf16_f32 v74, v13, s0
	ds_write_b16 v190, v74 offset:544
	v_cvt_pk_bf16_f32 v74, v14, s0
	ds_write_b16 v190, v74 offset:4080
	v_cvt_pk_bf16_f32 v74, v15, s0
	ds_write_b16 v190, v74 offset:4352
	v_cvt_pk_bf16_f32 v74, v16, s0
	ds_write_b16 v190, v74 offset:4624
	v_cvt_pk_bf16_f32 v74, v17, s0
	ds_write_b16 v190, v74 offset:4896
	v_cvt_pk_bf16_f32 v74, v6, s0
	ds_write_b16 v190, v74 offset:8432
	v_cvt_pk_bf16_f32 v74, v7, s0
	ds_write_b16 v190, v74 offset:8704
	v_cvt_pk_bf16_f32 v74, v8, s0
	ds_write_b16 v190, v74 offset:8976
	v_cvt_pk_bf16_f32 v74, v9, s0
	ds_write_b16 v190, v74 offset:9248
	v_cvt_pk_bf16_f32 v74, v2, s0
	ds_write_b16 v190, v74 offset:12784
	v_cvt_pk_bf16_f32 v74, v3, s0
	ds_write_b16 v190, v74 offset:13056
	v_cvt_pk_bf16_f32 v74, v4, s0
	ds_write_b16 v190, v74 offset:13328
	v_cvt_pk_bf16_f32 v74, v5, s0
	ds_write_b16 v190, v74 offset:13600
	v_lshlrev_b32_e32 v92, 16, v22
	v_and_b32_e32 v93, 0xffff0000, v22
	v_mul_f32_e32 v92, v227, v92
	v_mul_f32_e32 v93, v227, v93
	v_cvt_pk_bf16_f32 v84, v92, v93
	v_lshlrev_b32_e32 v92, 16, v23
	v_and_b32_e32 v93, 0xffff0000, v23
	v_mul_f32_e32 v92, v227, v92
	v_mul_f32_e32 v93, v227, v93
	v_cvt_pk_bf16_f32 v85, v92, v93
	v_lshlrev_b32_e32 v92, 16, v24
	v_and_b32_e32 v93, 0xffff0000, v24
	v_mul_f32_e32 v92, v227, v92
	v_mul_f32_e32 v93, v227, v93
	v_cvt_pk_bf16_f32 v86, v92, v93
	v_lshlrev_b32_e32 v92, 16, v25
	v_and_b32_e32 v93, 0xffff0000, v25
	v_mul_f32_e32 v92, v227, v92
	v_mul_f32_e32 v93, v227, v93
	v_cvt_pk_bf16_f32 v87, v92, v93
	ds_write_b128 v194, v[22:25]
	ds_write_b128 v195, v[84:87]
	v_lshlrev_b32_e32 v92, 16, v18
	v_and_b32_e32 v93, 0xffff0000, v18
	v_mul_f32_e32 v92, v227, v92
	v_mul_f32_e32 v93, v227, v93
	v_cvt_pk_bf16_f32 v88, v92, v93
	v_lshlrev_b32_e32 v92, 16, v19
	v_and_b32_e32 v93, 0xffff0000, v19
	v_mul_f32_e32 v92, v227, v92
	v_mul_f32_e32 v93, v227, v93
	v_cvt_pk_bf16_f32 v89, v92, v93
; #define LAS __attribute__((address_space(3)))
; __device__ __forceinline__ unsigned pk2(float lo, float hi) { unsigned r; asm volatile("v_cvt_pk_bf16_f32 %0, %1, %2" : "=v"(r) : "v"(lo), "v"(hi)); return r; }
; __device__ __forceinline__ float bflo(unsigned w) { return __uint_as_float(w << 16); }
; __device__ __forceinline__ float bfhi(unsigned w) { return __uint_as_float(w & 0xffff0000u); }
; template <int NET> __device__ __forceinline__ void ret_item(Ctx& F, int item) {
;     ...
;             for (int hh = 0; hh < 2; ++hh) { unsigned oq1[4], oq2[4], ok1[4], ok2[4];
; #pragma unroll
;                 for (int c = 0; c < 4; ++c) { float a[2], bq[2], ka[2], kb[2];
; #pragma unroll
;                     for (int z = 0; z < 2; ++z) { const int jj = hh * 8 + c * 2 + z; const unsigned cw_ = cs4[jj >> 2][jj & 3]; const f32x2 sc = (f32x2){bflo(cw_), bfhi(cw_)};
;                         const float x1 = z ? bfhi(q1[hh][c]) : bflo(q1[hh][c]), x2 = z ? bfhi(q2[hh][c]) : bflo(q2[hh][c]);
;                         const float y1 = z ? bfhi(k1[hh][c]) : bflo(k1[hh][c]), y2 = z ? bfhi(k2[hh][c]) : bflo(k2[hh][c]);
;                         a[z] = (x1 * sc.x - x2 * sc.y) * 0.08838834764831845f; bq[z] = (x2 * sc.x + x1 * sc.y) * 0.08838834764831845f;
;                         ka[z] = y1 * sc.x - y2 * sc.y; kb[z] = y2 * sc.x + y1 * sc.y;
;                     }
;                     oq1[c] = pk2(a[0], a[1]); oq2[c] = pk2(bq[0], bq[1]); ok1[c] = pk2(ka[0], ka[1]); ok2[c] = pk2(kb[0], kb[1]); }
;                 *(LAS u32x4*)(qL + r * LP + j0 + hh * 8) = (u32x4){oq1[0], oq1[1], oq1[2], oq1[3]}; *(LAS u32x4*)(qL + r * LP + 64 + j0 + hh * 8) = (u32x4){oq2[0], oq2[1], oq2[2], oq2[3]};
;                 *(LAS u32x4*)(kL + r * LP + j0 + hh * 8) = (u32x4){ok1[0], ok1[1], ok1[2], ok1[3]}; *(LAS u32x4*)(kL + r * LP + 64 + j0 + hh * 8) = (u32x4){ok2[0], ok2[1], ok2[2], ok2[3]}; }
; #pragma unroll
;             for (int vi = 0; vi < NET / 2; ++vi) { unsigned vd[4];
; #pragma unroll
;                 for (int c = 0; c < 4; ++c) vd[c] = pk2(bflo(vv[vi][c]) * kdec, bfhi(vv[vi][c]) * kdec);
;                 *(LAS u32x4*)(vL + r * VP + qd * (EW / 4) + 8 * vi) = vv[vi]; *(LAS u32x4*)(vdL + r * VP + qd * (EW / 4) + 8 * vi) = (u32x4){vd[0], vd[1], vd[2], vd[3]}; }
	v_lshlrev_b32_e32 v92, 16, v20
	v_and_b32_e32 v93, 0xffff0000, v20
	v_mul_f32_e32 v92, v227, v92
	v_mul_f32_e32 v93, v227, v93
	v_cvt_pk_bf16_f32 v90, v92, v93
	v_lshlrev_b32_e32 v92, 16, v21
	v_and_b32_e32 v93, 0xffff0000, v21
	v_mul_f32_e32 v92, v227, v92
	v_mul_f32_e32 v93, v227, v93
	v_cvt_pk_bf16_f32 v91, v92, v93
	ds_write_b128 v194, v[18:21] offset:16
	ds_write_b128 v195, v[88:91] offset:16
	v_cvt_pk_bf16_f32 v62, v80, v50
	v_cvt_pk_bf16_f32 v58, v81, v54
	v_cvt_pk_bf16_f32 v54, v82, v76
	v_cvt_pk_bf16_f32 v50, v83, v70
	v_and_b32_e32 v70, 0xffff0000, v72
	v_lshlrev_b32_e32 v71, 16, v72
	v_lshlrev_b32_e32 v77, 16, v55
	v_lshlrev_b32_e32 v76, 16, v51
	v_pk_mul_f32 v[78:79], v[70:71], v[76:77] op_sel:[1,0] op_sel_hi:[0,1]
	v_lshlrev_b32_e32 v75, 16, v63
	v_lshlrev_b32_e32 v74, 16, v59
	v_sub_f32_e32 v72, v78, v79
	v_pk_mul_f32 v[76:77], v[76:77], v[70:71]
	v_mul_f32_e32 v78, 0x3db504f3, v72
	v_add_f32_e32 v72, v76, v77
	v_pk_mul_f32 v[76:77], v[70:71], v[74:75] op_sel:[1,0] op_sel_hi:[0,1]
	v_pk_mul_f32 v[70:71], v[74:75], v[70:71]
	v_and_b32_e32 v75, 0xffff0000, v55
	v_add_f32_e32 v81, v70, v71
	v_and_b32_e32 v70, 0xffff0000, v73
	v_lshlrev_b32_e32 v71, 16, v73
	v_and_b32_e32 v74, 0xffff0000, v51
	v_mul_f32_e32 v79, 0x3db504f3, v72
	v_sub_f32_e32 v80, v76, v77
	v_and_b32_e32 v73, 0xffff0000, v63
	v_and_b32_e32 v72, 0xffff0000, v59
	v_pk_mul_f32 v[76:77], v[70:71], v[74:75] op_sel:[1,0] op_sel_hi:[0,1]
	v_pk_mul_f32 v[74:75], v[74:75], v[70:71]
	v_sub_f32_e32 v51, v76, v77
	v_add_f32_e32 v55, v74, v75
	v_pk_mul_f32 v[74:75], v[70:71], v[72:73] op_sel:[1,0] op_sel_hi:[0,1]
	v_pk_mul_f32 v[70:71], v[72:73], v[70:71]
	v_mul_f32_e32 v51, 0x3db504f3, v51
	v_mul_f32_e32 v55, 0x3db504f3, v55
	v_sub_f32_e32 v74, v74, v75
	v_add_f32_e32 v70, v70, v71
	v_cvt_pk_bf16_f32 v63, v78, v51
	v_cvt_pk_bf16_f32 v59, v79, v55
	v_cvt_pk_bf16_f32 v55, v80, v74
	v_cvt_pk_bf16_f32 v51, v81, v70
	v_and_b32_e32 v70, 0xffff0000, v66
	v_lshlrev_b32_e32 v71, 16, v66
	v_lshlrev_b32_e32 v75, 16, v56
	v_lshlrev_b32_e32 v74, 16, v52
	v_pk_mul_f32 v[76:77], v[70:71], v[74:75] op_sel:[1,0] op_sel_hi:[0,1]
	v_sub_f32_e32 v66, v76, v77
	v_pk_mul_f32 v[74:75], v[74:75], v[70:71]
	v_lshlrev_b32_e32 v73, 16, v64
	v_lshlrev_b32_e32 v72, 16, v60
	v_mul_f32_e32 v76, 0x3db504f3, v66
	v_add_f32_e32 v66, v74, v75
	v_mul_f32_e32 v77, 0x3db504f3, v66
	v_pk_mul_f32 v[74:75], v[70:71], v[72:73] op_sel:[1,0] op_sel_hi:[0,1]
	v_pk_mul_f32 v[70:71], v[72:73], v[70:71]
	v_and_b32_e32 v66, 0xffff0000, v67
	v_lshlrev_b32_e32 v67, 16, v67
	v_and_b32_e32 v73, 0xffff0000, v56
	v_and_b32_e32 v72, 0xffff0000, v52
	v_sub_f32_e32 v78, v74, v75
	v_add_f32_e32 v79, v70, v71
	v_and_b32_e32 v71, 0xffff0000, v64
	v_and_b32_e32 v70, 0xffff0000, v60
	v_pk_mul_f32 v[74:75], v[66:67], v[72:73] op_sel:[1,0] op_sel_hi:[0,1]
	v_pk_mul_f32 v[72:73], v[72:73], v[66:67]
	v_sub_f32_e32 v52, v74, v75
	v_add_f32_e32 v56, v72, v73
	v_pk_mul_f32 v[72:73], v[66:67], v[70:71] op_sel:[1,0] op_sel_hi:[0,1]
	v_pk_mul_f32 v[66:67], v[70:71], v[66:67]
	v_mul_f32_e32 v52, 0x3db504f3, v52
	v_mul_f32_e32 v56, 0x3db504f3, v56
	v_sub_f32_e32 v72, v72, v73
	v_add_f32_e32 v66, v66, v67
	v_cvt_pk_bf16_f32 v64, v76, v52
	v_cvt_pk_bf16_f32 v60, v77, v56
	v_cvt_pk_bf16_f32 v56, v78, v72
	v_cvt_pk_bf16_f32 v52, v79, v66
	v_and_b32_e32 v66, 0xffff0000, v68
	v_lshlrev_b32_e32 v67, 16, v68
	v_lshlrev_b32_e32 v73, 16, v57
	v_lshlrev_b32_e32 v72, 16, v53
	v_pk_mul_f32 v[74:75], v[66:67], v[72:73] op_sel:[1,0] op_sel_hi:[0,1]
	v_lshlrev_b32_e32 v71, 16, v65
	v_lshlrev_b32_e32 v70, 16, v61
	v_sub_f32_e32 v68, v74, v75
	v_pk_mul_f32 v[72:73], v[72:73], v[66:67]
	v_mul_f32_e32 v74, 0x3db504f3, v68
	v_add_f32_e32 v68, v72, v73
	v_pk_mul_f32 v[72:73], v[66:67], v[70:71] op_sel:[1,0] op_sel_hi:[0,1]
	v_pk_mul_f32 v[66:67], v[70:71], v[66:67]
	v_and_b32_e32 v71, 0xffff0000, v57
	v_add_f32_e32 v77, v66, v67
	v_and_b32_e32 v66, 0xffff0000, v69
	v_lshlrev_b32_e32 v67, 16, v69
	v_and_b32_e32 v70, 0xffff0000, v53
	v_sub_f32_e32 v76, v72, v73
	v_pk_mul_f32 v[72:73], v[66:67], v[70:71] op_sel:[1,0] op_sel_hi:[0,1]
	v_pk_mul_f32 v[70:71], v[70:71], v[66:67]
	v_mul_f32_e32 v75, 0x3db504f3, v68
	v_and_b32_e32 v69, 0xffff0000, v65
	v_and_b32_e32 v68, 0xffff0000, v61
	v_sub_f32_e32 v53, v72, v73
	v_add_f32_e32 v57, v70, v71
	v_mul_f32_e32 v53, 0x3db504f3, v53
	v_mul_f32_e32 v57, 0x3db504f3, v57
	v_pk_mul_f32 v[70:71], v[66:67], v[68:69] op_sel:[1,0] op_sel_hi:[0,1]
	v_pk_mul_f32 v[66:67], v[68:69], v[66:67]
	v_sub_f32_e32 v70, v70, v71
	v_add_f32_e32 v66, v66, v67
	v_cvt_pk_bf16_f32 v65, v74, v53
	v_cvt_pk_bf16_f32 v61, v75, v57
	v_cvt_pk_bf16_f32 v57, v76, v70
	v_cvt_pk_bf16_f32 v53, v77, v66
	ds_write_b128 v161, v[62:65]
	ds_write_b128 v161, v[58:61] offset:128
	ds_write_b128 v161, v[54:57] offset:34816
	ds_write_b128 v161, v[50:53] offset:34944
	v_lshlrev_b32_e32 v50, 16, v46
	v_and_b32_e32 v51, 0xffff0000, v46
	v_lshlrev_b32_e32 v53, 16, v30
	v_lshlrev_b32_e32 v52, 16, v26
	v_pk_mul_f32 v[54:55], v[52:53], v[50:51]
	v_pk_mul_f32 v[52:53], v[50:51], v[52:53] op_sel:[1,0] op_sel_hi:[0,1]
	v_sub_f32_e32 v46, v54, v55
	v_mul_f32_e32 v56, 0x3db504f3, v46
	v_add_f32_e32 v46, v52, v53
	v_lshlrev_b32_e32 v53, 16, v38
	v_lshlrev_b32_e32 v52, 16, v34
	v_pk_mul_f32 v[54:55], v[52:53], v[50:51]
	v_pk_mul_f32 v[50:51], v[50:51], v[52:53] op_sel:[1,0] op_sel_hi:[0,1]
; #define LAS __attribute__((address_space(3)))
; __device__ __forceinline__ unsigned pk2(float lo, float hi) { unsigned r; asm volatile("v_cvt_pk_bf16_f32 %0, %1, %2" : "=v"(r) : "v"(lo), "v"(hi)); return r; }
; __device__ __forceinline__ float bflo(unsigned w) { return __uint_as_float(w << 16); }
; __device__ __forceinline__ float bfhi(unsigned w) { return __uint_as_float(w & 0xffff0000u); }
; template <int NET> __device__ __forceinline__ void ret_item(Ctx& F, int item) {
;     ...
;             for (int hh = 0; hh < 2; ++hh) { unsigned oq1[4], oq2[4], ok1[4], ok2[4];
; #pragma unroll
;                 for (int c = 0; c < 4; ++c) { float a[2], bq[2], ka[2], kb[2];
; #pragma unroll
;                     for (int z = 0; z < 2; ++z) { const int jj = hh * 8 + c * 2 + z; const unsigned cw_ = cs4[jj >> 2][jj & 3]; const f32x2 sc = (f32x2){bflo(cw_), bfhi(cw_)};
;                         const float x1 = z ? bfhi(q1[hh][c]) : bflo(q1[hh][c]), x2 = z ? bfhi(q2[hh][c]) : bflo(q2[hh][c]);
;                         const float y1 = z ? bfhi(k1[hh][c]) : bflo(k1[hh][c]), y2 = z ? bfhi(k2[hh][c]) : bflo(k2[hh][c]);
;                         a[z] = (x1 * sc.x - x2 * sc.y) * 0.08838834764831845f; bq[z] = (x2 * sc.x + x1 * sc.y) * 0.08838834764831845f;
;                         ka[z] = y1 * sc.x - y2 * sc.y; kb[z] = y2 * sc.x + y1 * sc.y;
;                     }
;                     oq1[c] = pk2(a[0], a[1]); oq2[c] = pk2(bq[0], bq[1]); ok1[c] = pk2(ka[0], ka[1]); ok2[c] = pk2(kb[0], kb[1]); }
;                 *(LAS u32x4*)(qL + r * LP + j0 + hh * 8) = (u32x4){oq1[0], oq1[1], oq1[2], oq1[3]}; *(LAS u32x4*)(qL + r * LP + 64 + j0 + hh * 8) = (u32x4){oq2[0], oq2[1], oq2[2], oq2[3]};
;                 *(LAS u32x4*)(kL + r * LP + j0 + hh * 8) = (u32x4){ok1[0], ok1[1], ok1[2], ok1[3]}; *(LAS u32x4*)(kL + r * LP + 64 + j0 + hh * 8) = (u32x4){ok2[0], ok2[1], ok2[2], ok2[3]}; }
; __global__ void __launch_bounds__(NWAVES * 64, 2) fwd_kernel(Args args) {
;     ...
;             if (!split || (F.vcu & 1) == 0) { for (int it = hw; it < NB * 8 * 2; it += HS) ret_item<4>(F, it); }
	v_mul_f32_e32 v57, 0x3db504f3, v46
	v_sub_f32_e32 v54, v54, v55
	v_add_f32_e32 v55, v50, v51
	v_lshlrev_b32_e32 v46, 16, v47
	v_and_b32_e32 v47, 0xffff0000, v47
	v_and_b32_e32 v51, 0xffff0000, v30
	v_and_b32_e32 v50, 0xffff0000, v26
	v_pk_mul_f32 v[52:53], v[50:51], v[46:47]
	v_pk_mul_f32 v[50:51], v[46:47], v[50:51] op_sel:[1,0] op_sel_hi:[0,1]
	v_add_f32_e32 v30, v50, v51
	v_and_b32_e32 v51, 0xffff0000, v38
	v_and_b32_e32 v50, 0xffff0000, v34
	v_sub_f32_e32 v26, v52, v53
	v_pk_mul_f32 v[52:53], v[50:51], v[46:47]
	v_pk_mul_f32 v[46:47], v[46:47], v[50:51] op_sel:[1,0] op_sel_hi:[0,1]
	v_mul_f32_e32 v26, 0x3db504f3, v26
	v_mul_f32_e32 v30, 0x3db504f3, v30
	v_add_f32_e32 v46, v46, v47
	v_sub_f32_e32 v52, v52, v53
	v_cvt_pk_bf16_f32 v38, v56, v26
	v_cvt_pk_bf16_f32 v34, v57, v30
	v_cvt_pk_bf16_f32 v30, v54, v52
	v_cvt_pk_bf16_f32 v26, v55, v46
	v_lshlrev_b32_e32 v46, 16, v48
	v_and_b32_e32 v47, 0xffff0000, v48
	v_lshlrev_b32_e32 v51, 16, v31
	v_lshlrev_b32_e32 v50, 16, v27
	v_pk_mul_f32 v[52:53], v[50:51], v[46:47]
	v_pk_mul_f32 v[50:51], v[46:47], v[50:51] op_sel:[1,0] op_sel_hi:[0,1]
	v_sub_f32_e32 v48, v52, v53
	v_mul_f32_e32 v54, 0x3db504f3, v48
	v_add_f32_e32 v48, v50, v51
	v_lshlrev_b32_e32 v51, 16, v39
	v_lshlrev_b32_e32 v50, 16, v35
	v_pk_mul_f32 v[52:53], v[50:51], v[46:47]
	v_pk_mul_f32 v[46:47], v[46:47], v[50:51] op_sel:[1,0] op_sel_hi:[0,1]
	v_mul_f32_e32 v55, 0x3db504f3, v48
	v_sub_f32_e32 v52, v52, v53
	v_add_f32_e32 v53, v46, v47
	v_lshlrev_b32_e32 v46, 16, v49
	v_and_b32_e32 v47, 0xffff0000, v49
	v_and_b32_e32 v49, 0xffff0000, v31
	v_and_b32_e32 v48, 0xffff0000, v27
	v_pk_mul_f32 v[50:51], v[48:49], v[46:47]
	v_pk_mul_f32 v[48:49], v[46:47], v[48:49] op_sel:[1,0] op_sel_hi:[0,1]
	v_add_f32_e32 v31, v48, v49
	v_and_b32_e32 v49, 0xffff0000, v39
	v_and_b32_e32 v48, 0xffff0000, v35
	v_sub_f32_e32 v27, v50, v51
	v_pk_mul_f32 v[50:51], v[48:49], v[46:47]
	v_pk_mul_f32 v[46:47], v[46:47], v[48:49] op_sel:[1,0] op_sel_hi:[0,1]
	v_mul_f32_e32 v27, 0x3db504f3, v27
	v_mul_f32_e32 v31, 0x3db504f3, v31
	v_add_f32_e32 v46, v46, v47
	v_sub_f32_e32 v50, v50, v51
	v_cvt_pk_bf16_f32 v39, v54, v27
	v_cvt_pk_bf16_f32 v35, v55, v31
	v_cvt_pk_bf16_f32 v31, v52, v50
	v_cvt_pk_bf16_f32 v27, v53, v46
	v_lshlrev_b32_e32 v46, 16, v42
	v_and_b32_e32 v47, 0xffff0000, v42
	v_lshlrev_b32_e32 v49, 16, v32
	v_lshlrev_b32_e32 v48, 16, v28
	v_pk_mul_f32 v[50:51], v[48:49], v[46:47]
	v_pk_mul_f32 v[48:49], v[46:47], v[48:49] op_sel:[1,0] op_sel_hi:[0,1]
	v_sub_f32_e32 v42, v50, v51
	v_mul_f32_e32 v52, 0x3db504f3, v42
	v_add_f32_e32 v42, v48, v49
	v_lshlrev_b32_e32 v49, 16, v40
	v_lshlrev_b32_e32 v48, 16, v36
	v_pk_mul_f32 v[50:51], v[48:49], v[46:47]
	v_pk_mul_f32 v[46:47], v[46:47], v[48:49] op_sel:[1,0] op_sel_hi:[0,1]
	v_mul_f32_e32 v53, 0x3db504f3, v42
	v_sub_f32_e32 v50, v50, v51
	v_add_f32_e32 v51, v46, v47
	v_lshlrev_b32_e32 v42, 16, v43
	v_and_b32_e32 v43, 0xffff0000, v43
	v_and_b32_e32 v47, 0xffff0000, v32
	v_and_b32_e32 v46, 0xffff0000, v28
	v_pk_mul_f32 v[48:49], v[46:47], v[42:43]
	v_pk_mul_f32 v[46:47], v[42:43], v[46:47] op_sel:[1,0] op_sel_hi:[0,1]
	v_add_f32_e32 v32, v46, v47
	v_and_b32_e32 v47, 0xffff0000, v40
	v_and_b32_e32 v46, 0xffff0000, v36
	v_sub_f32_e32 v28, v48, v49
	v_pk_mul_f32 v[48:49], v[46:47], v[42:43]
	v_pk_mul_f32 v[42:43], v[42:43], v[46:47] op_sel:[1,0] op_sel_hi:[0,1]
	v_mul_f32_e32 v28, 0x3db504f3, v28
	v_mul_f32_e32 v32, 0x3db504f3, v32
	v_add_f32_e32 v42, v42, v43
	v_sub_f32_e32 v48, v48, v49
	v_cvt_pk_bf16_f32 v40, v52, v28
	v_cvt_pk_bf16_f32 v36, v53, v32
	v_cvt_pk_bf16_f32 v32, v50, v48
	v_cvt_pk_bf16_f32 v28, v51, v42
	v_and_b32_e32 v42, 0xffff0000, v44
	v_lshlrev_b32_e32 v43, 16, v44
	v_lshlrev_b32_e32 v47, 16, v41
	v_lshlrev_b32_e32 v46, 16, v37
	v_pk_mul_f32 v[48:49], v[46:47], v[42:43]
	v_pk_mul_f32 v[46:47], v[42:43], v[46:47] op_sel:[1,0] op_sel_hi:[0,1]
	v_add_f32_e32 v48, v48, v49
	v_sub_f32_e32 v49, v46, v47
	v_lshlrev_b32_e32 v47, 16, v33
	v_lshlrev_b32_e32 v46, 16, v29
	v_pk_mul_f32 v[50:51], v[46:47], v[42:43]
	v_pk_mul_f32 v[42:43], v[42:43], v[46:47] op_sel:[1,0] op_sel_hi:[0,1]
	v_add_f32_e32 v44, v50, v51
	v_mul_f32_e32 v50, 0x3db504f3, v44
	v_and_b32_e32 v44, 0xffff0000, v45
	v_lshlrev_b32_e32 v45, 16, v45
	v_and_b32_e32 v47, 0xffff0000, v33
	v_and_b32_e32 v46, 0xffff0000, v29
	v_sub_f32_e32 v42, v42, v43
	v_pk_mul_f32 v[52:53], v[44:45], v[46:47] op_sel:[1,0] op_sel_hi:[0,1]
	v_pk_mul_f32 v[46:47], v[46:47], v[44:45]
	v_mul_f32_e32 v51, 0x3db504f3, v42
	v_and_b32_e32 v43, 0xffff0000, v41
	v_and_b32_e32 v42, 0xffff0000, v37
	v_sub_f32_e32 v29, v52, v53
	v_add_f32_e32 v33, v46, v47
	v_mul_f32_e32 v29, 0x3db504f3, v29
	v_mul_f32_e32 v33, 0x3db504f3, v33
	v_pk_mul_f32 v[46:47], v[44:45], v[42:43] op_sel:[1,0] op_sel_hi:[0,1]
	v_pk_mul_f32 v[42:43], v[42:43], v[44:45]
	v_cvt_pk_bf16_f32 v41, v51, v29
	v_sub_f32_e32 v46, v46, v47
	v_add_f32_e32 v42, v42, v43
	v_cvt_pk_bf16_f32 v37, v50, v33
	v_cvt_pk_bf16_f32 v33, v49, v46
	v_cvt_pk_bf16_f32 v29, v48, v42
	ds_write_b128 v161, v[38:41] offset:16
	ds_write_b128 v161, v[34:37] offset:144
	ds_write_b128 v161, v[30:33] offset:34832
	ds_write_b128 v161, v[26:29] offset:34960
	s_cbranch_scc1 .LBB0_314
	s_add_i32 s93, s93, s3
	s_cmpk_lt_i32 s93, 0x80
	s_waitcnt lgkmcnt(0)
	s_barrier
	s_cbranch_scc1 .LBB0_311
